# adds window-unit per-wave skip of QK^T + band mask for key tiles entirely outside the wave's band (on top of the NA dead-tile skip)
# speedup vs baseline: 1.0036x; 1.0036x over previous
.LBB0_640:
	s_add_i32 s26, s27, 2
	s_add_i32 s2, s5, s25
	s_addk_i32 s2, 0xff00
	s_add_i32 s3, s2, 0x5e
	s_sub_i32 s2, s2, 0x5e
	v_cmp_lt_i32_e32 vcc, s3, v175
	v_cmp_gt_i32_e64 s[2:3], s2, v176
	s_nop 1
	s_or_b64 s[2:3], vcc, s[2:3]
	s_cmp_ge_i32 s26, s20
	s_cselect_b64 s[2:3], 0, s[2:3]
	s_cmp_eq_u64 s[2:3], exec
	s_cbranch_scc1 .Lwin_deadA
	ds_read_b128 v[64:67], v166 offset:49152
	ds_read_b128 v[230:233], v168 offset:49152
	ds_read_b128 v[234:237], v166 offset:57344
	ds_read_b128 v[238:241], v168 offset:57344
	v_add_f32_e32 v144, 0, v191
	v_add_f32_e32 v144, v201, v144
	v_add_f32_e32 v144, v145, v144
	v_add_f32_e32 v144, v200, v144
	v_add_f32_e32 v144, v146, v144
	v_add_f32_e32 v144, v190, v144
	v_add_f32_e32 v144, v147, v144
	v_add_f32_e32 v144, v189, v144
	v_add_f32_e32 v144, v186, v144
	v_add_f32_e32 v144, v188, v144
	v_add_f32_e32 v144, v185, v144
	v_add_f32_e32 v144, v187, v144
	v_exp_f32_e32 v142, v142
	v_add_f32_e32 v144, v182, v144
	v_exp_f32_e32 v143, v143
	v_add_f32_e32 v144, v184, v144
	v_exp_f32_e32 v140, v140
	v_add_f32_e32 v144, v181, v144
	v_exp_f32_e32 v141, v141
	v_add_f32_e32 v144, v183, v144
	v_exp_f32_e32 v138, v138
	v_add_f32_e32 v144, v142, v144
	v_exp_f32_e32 v139, v139
	v_add_f32_e32 v144, v143, v144
	v_exp_f32_e32 v136, v136
	v_add_f32_e32 v144, v140, v144
	v_exp_f32_e32 v137, v137
	v_add_f32_e32 v144, v141, v144
	v_exp_f32_e32 v134, v134
	v_add_f32_e32 v144, v138, v144
	v_exp_f32_e32 v135, v135
	v_add_f32_e32 v144, v139, v144
	v_exp_f32_e32 v132, v132
	v_add_f32_e32 v144, v136, v144
	v_exp_f32_e32 v133, v133
	v_add_f32_e32 v144, v137, v144
	v_exp_f32_e32 v130, v130
	v_add_f32_e32 v144, v134, v144
	v_exp_f32_e32 v131, v131
	v_add_f32_e32 v144, v135, v144
	v_exp_f32_e32 v128, v128
	v_add_f32_e32 v144, v132, v144
	v_exp_f32_e32 v129, v129
	v_add_f32_e32 v144, v133, v144
	v_add_f32_e32 v144, v130, v144
	v_add_f32_e32 v144, v131, v144
	v_add_f32_e32 v144, v128, v144
	v_add_f32_e32 v179, v129, v144
	v_mov_b32_e32 v180, v179
	v_cvt_pk_bf16_f32 v144, v191, v201
	v_cvt_pk_bf16_f32 v145, v145, v200
	v_cvt_pk_bf16_f32 v146, v146, v190
	v_cvt_pk_bf16_f32 v147, v147, v189
	v_cvt_pk_bf16_f32 v186, v186, v188
	v_cvt_pk_bf16_f32 v187, v185, v187
	v_cvt_pk_bf16_f32 v188, v182, v184
	v_cvt_pk_bf16_f32 v189, v181, v183
	v_cvt_pk_bf16_f32 v182, v142, v143
	v_cvt_pk_bf16_f32 v183, v140, v141
	v_cvt_pk_bf16_f32 v184, v138, v139
	v_cvt_pk_bf16_f32 v185, v136, v137
	v_cvt_pk_bf16_f32 v200, v134, v135
	v_cvt_pk_bf16_f32 v201, v132, v133
	v_cvt_pk_bf16_f32 v202, v130, v131
	s_nop 0
	v_permlane32_swap_b32_e32 v179, v180
	v_permlane32_swap_b32_e32 v144, v146
	v_cvt_pk_bf16_f32 v203, v128, v129
	v_permlane32_swap_b32_e32 v200, v202
	v_permlane32_swap_b32_e32 v145, v147
	v_permlane32_swap_b32_e32 v186, v188
	v_permlane32_swap_b32_e32 v187, v189
	v_permlane32_swap_b32_e32 v182, v184
	v_permlane32_swap_b32_e32 v183, v185
	v_permlane32_swap_b32_e32 v201, v203
	s_add_i32 s2, s27, 3
	s_cmp_lt_i32 s2, s20
	s_cselect_b64 s[8:9], -1, 0
	s_and_b64 s[2:3], s[8:9], exec
	s_cselect_b32 s2, 0, s20
	s_cselect_b32 s3, s19, 0x4000
	s_lshl_b32 s2, s2, 6
	s_sub_i32 s2, s3, s2
	s_add_i32 s2, s25, s2
	s_mulk_i32 s2, 0x2400
	s_add_i32 s10, s2, 0xfff70000
	s_add_u32 s2, s21, s10
	s_addc_u32 s3, s22, 0
	s_add_u32 s10, s23, s10
	s_addc_u32 s11, s24, 0
	v_lshl_add_u64 v[128:129], s[10:11], 0, v[192:193]
	v_lshl_add_u64 v[132:133], s[10:11], 0, v[152:153]
	v_lshl_add_u64 v[136:137], s[2:3], 0, v[192:193]
	v_lshl_add_u64 v[140:141], s[2:3], 0, v[152:153]
	global_load_dwordx4 v[128:131], v[128:129], off
	s_nop 0
	global_load_dwordx4 v[132:135], v[132:133], off
	s_nop 0
	global_load_dwordx4 v[136:139], v[136:137], off
	s_nop 0
	global_load_dwordx4 v[140:143], v[140:141], off
	s_cmp_ge_i32 s26, s20
	s_waitcnt lgkmcnt(3)
	v_mfma_f32_32x32x16_bf16 v[80:95], v[64:67], v[124:127], 0
	s_waitcnt lgkmcnt(2)
	v_mfma_f32_32x32x16_bf16 v[80:95], v[230:233], v[120:123], v[80:95]
	ds_read_b128 v[230:233], v167 offset:49152
	s_waitcnt lgkmcnt(2)
	v_mfma_f32_32x32x16_bf16 v[64:79], v[234:237], v[124:127], 0
	ds_read_b128 v[234:237], v167 offset:57344
	s_waitcnt lgkmcnt(2)
	v_mfma_f32_32x32x16_bf16 v[64:79], v[238:241], v[120:123], v[64:79]
	ds_read_b128 v[238:241], v165 offset:49152
	s_waitcnt lgkmcnt(2)
	v_mfma_f32_32x32x16_bf16 v[80:95], v[230:233], v[116:119], v[80:95]
	ds_read_b128 v[230:233], v165 offset:57344
	s_waitcnt lgkmcnt(2)
	v_mfma_f32_32x32x16_bf16 v[64:79], v[234:237], v[116:119], v[64:79]
	ds_read_b128 v[234:237], v164 offset:49152
	s_waitcnt lgkmcnt(2)
	v_mfma_f32_32x32x16_bf16 v[80:95], v[238:241], v[112:115], v[80:95]
	ds_read_b128 v[238:241], v164 offset:57344
	s_waitcnt lgkmcnt(2)
	v_mfma_f32_32x32x16_bf16 v[64:79], v[230:233], v[112:115], v[64:79]
	ds_read_b128 v[230:233], v163 offset:49152
	s_waitcnt lgkmcnt(2)
	v_mfma_f32_32x32x16_bf16 v[80:95], v[234:237], v[108:111], v[80:95]
	ds_read_b128 v[234:237], v163 offset:57344
	s_waitcnt lgkmcnt(2)
	v_mfma_f32_32x32x16_bf16 v[64:79], v[238:241], v[108:111], v[64:79]
	ds_read_b128 v[238:241], v162 offset:49152
	s_waitcnt lgkmcnt(2)
	v_mfma_f32_32x32x16_bf16 v[80:95], v[230:233], v[104:107], v[80:95]
	ds_read_b128 v[230:233], v162 offset:57344
	s_waitcnt lgkmcnt(2)
	v_mfma_f32_32x32x16_bf16 v[64:79], v[234:237], v[104:107], v[64:79]
	ds_read_b128 v[234:237], v161 offset:49152
	s_waitcnt lgkmcnt(2)
	v_mfma_f32_32x32x16_bf16 v[80:95], v[238:241], v[100:103], v[80:95]
	ds_read_b128 v[238:241], v161 offset:57344
	s_waitcnt lgkmcnt(2)
	v_mfma_f32_32x32x16_bf16 v[64:79], v[230:233], v[100:103], v[64:79]
	s_waitcnt lgkmcnt(1)
	v_mfma_f32_32x32x16_bf16 v[80:95], v[234:237], v[96:99], v[80:95]
	s_waitcnt lgkmcnt(0)
	v_mfma_f32_32x32x16_bf16 v[64:79], v[238:241], v[96:99], v[64:79]
	s_cbranch_scc1 .LBB0_644
	s_add_i32 s2, s5, s25
	s_addk_i32 s2, 0xff00
	v_cmp_lt_i32_e32 vcc, s2, v175
	v_cmp_gt_i32_e64 s[2:3], s2, v176
	s_or_b64 s[8:9], vcc, s[2:3]
	s_and_saveexec_b64 s[2:3], s[8:9]
	s_cbranch_execz .LBB0_643
	v_add_u32_e32 v242, s25, v178
	v_add_u32_e32 v243, 0xffffff80, v242
	s_movk_i32 s8, 0x101
	v_cmp_gt_u32_e32 vcc, s8, v243
	v_add_u32_e32 v243, 0xffffffa0, v242
	s_nop 0
	v_cndmask_b32_e32 v80, v217, v80, vcc
	v_cmp_gt_u32_e32 vcc, s8, v243
	v_add_u32_e32 v243, 0xffffff81, v242
	s_nop 0
	v_cndmask_b32_e32 v64, v217, v64, vcc
	v_cmp_gt_u32_e32 vcc, s8, v243
	v_add_u32_e32 v243, 0xffffffa1, v242
	s_nop 0
	v_cndmask_b32_e32 v81, v217, v81, vcc
	v_cmp_gt_u32_e32 vcc, s8, v243
	v_add_u32_e32 v243, 0xffffff82, v242
	s_nop 0
	v_cndmask_b32_e32 v65, v217, v65, vcc
	v_cmp_gt_u32_e32 vcc, s8, v243
	v_add_u32_e32 v243, 0xffffffa2, v242
	s_nop 0
	v_cndmask_b32_e32 v82, v217, v82, vcc
	v_cmp_gt_u32_e32 vcc, s8, v243
	v_add_u32_e32 v243, 0xffffff83, v242
	s_nop 0
	v_cndmask_b32_e32 v66, v217, v66, vcc
	v_cmp_gt_u32_e32 vcc, s8, v243
	v_add_u32_e32 v243, 0xffffffa3, v242
	s_nop 0
	v_cndmask_b32_e32 v83, v217, v83, vcc
	v_cmp_gt_u32_e32 vcc, s8, v243
	v_add_u32_e32 v243, 0xffffff88, v242
	s_nop 0
	v_cndmask_b32_e32 v67, v217, v67, vcc
	v_cmp_gt_u32_e32 vcc, s8, v243
	v_add_u32_e32 v243, 0xffffffa8, v242
	s_nop 0
	v_cndmask_b32_e32 v84, v217, v84, vcc
	v_cmp_gt_u32_e32 vcc, s8, v243
	v_add_u32_e32 v243, 0xffffff89, v242
	s_nop 0
	v_cndmask_b32_e32 v68, v217, v68, vcc
	v_cmp_gt_u32_e32 vcc, s8, v243
	v_add_u32_e32 v243, 0xffffffa9, v242
	s_nop 0
	v_cndmask_b32_e32 v85, v217, v85, vcc
	v_cmp_gt_u32_e32 vcc, s8, v243
	v_add_u32_e32 v243, 0xffffff8a, v242
	s_nop 0
	v_cndmask_b32_e32 v69, v217, v69, vcc
	v_cmp_gt_u32_e32 vcc, s8, v243
	v_add_u32_e32 v243, 0xffffffaa, v242
	s_nop 0
	v_cndmask_b32_e32 v86, v217, v86, vcc
	v_cmp_gt_u32_e32 vcc, s8, v243
	v_add_u32_e32 v243, 0xffffff8b, v242
	s_nop 0
	v_cndmask_b32_e32 v70, v217, v70, vcc
	v_cmp_gt_u32_e32 vcc, s8, v243
	v_add_u32_e32 v243, 0xffffffab, v242
	s_nop 0
	v_cndmask_b32_e32 v87, v217, v87, vcc
	v_cmp_gt_u32_e32 vcc, s8, v243
	v_add_u32_e32 v243, 0xffffff90, v242
	s_nop 0
	v_cndmask_b32_e32 v71, v217, v71, vcc
	v_cmp_gt_u32_e32 vcc, s8, v243
	v_add_u32_e32 v243, 0xffffffb0, v242
	s_nop 0
	v_cndmask_b32_e32 v88, v217, v88, vcc
	v_cmp_gt_u32_e32 vcc, s8, v243
	v_add_u32_e32 v243, 0xffffff91, v242
	s_nop 0
	v_cndmask_b32_e32 v72, v217, v72, vcc
	v_cmp_gt_u32_e32 vcc, s8, v243
	v_add_u32_e32 v243, 0xffffffb1, v242
	s_nop 0
	v_cndmask_b32_e32 v89, v217, v89, vcc
	v_cmp_gt_u32_e32 vcc, s8, v243
	v_add_u32_e32 v243, 0xffffff92, v242
	s_nop 0
	v_cndmask_b32_e32 v73, v217, v73, vcc
	v_cmp_gt_u32_e32 vcc, s8, v243
	v_add_u32_e32 v243, 0xffffffb2, v242
	s_nop 0
	v_cndmask_b32_e32 v90, v217, v90, vcc
	v_cmp_gt_u32_e32 vcc, s8, v243
	v_add_u32_e32 v243, 0xffffff93, v242
	s_nop 0
	v_cndmask_b32_e32 v74, v217, v74, vcc
	v_cmp_gt_u32_e32 vcc, s8, v243
	v_add_u32_e32 v243, 0xffffffb3, v242
	s_nop 0
	v_cndmask_b32_e32 v91, v217, v91, vcc
	v_cmp_gt_u32_e32 vcc, s8, v243
	v_add_u32_e32 v243, 0xffffff98, v242
	s_nop 0
	v_cndmask_b32_e32 v75, v217, v75, vcc
	v_cmp_gt_u32_e32 vcc, s8, v243
	v_add_u32_e32 v243, 0xffffffb8, v242
	s_nop 0
	v_cndmask_b32_e32 v92, v217, v92, vcc
	v_cmp_gt_u32_e32 vcc, s8, v243
	v_add_u32_e32 v243, 0xffffff99, v242
	s_nop 0
	v_cndmask_b32_e32 v76, v217, v76, vcc
	v_cmp_gt_u32_e32 vcc, s8, v243
	v_add_u32_e32 v243, 0xffffffb9, v242
	s_nop 0
	v_cndmask_b32_e32 v93, v217, v93, vcc
	v_cmp_gt_u32_e32 vcc, s8, v243
	v_add_u32_e32 v243, 0xffffff9a, v242
	s_nop 0
	v_cndmask_b32_e32 v77, v217, v77, vcc
	v_cmp_gt_u32_e32 vcc, s8, v243
	v_add_u32_e32 v243, 0xffffffba, v242
	s_nop 0
	v_cndmask_b32_e32 v94, v217, v94, vcc
	v_cmp_gt_u32_e32 vcc, s8, v243
	v_add_u32_e32 v243, 0xffffff9b, v242
	v_add_u32_e32 v242, 0xffffffbb, v242
	v_cndmask_b32_e32 v78, v217, v78, vcc
	v_cmp_gt_u32_e32 vcc, s8, v243
	s_nop 1
	v_cndmask_b32_e32 v95, v217, v95, vcc
	v_cmp_gt_u32_e32 vcc, s8, v242
	s_nop 1
	v_cndmask_b32_e32 v79, v217, v79, vcc

.LBB0_648:
	v_cndmask_b32_e64 v174, v144, v174, s[2:3]
	v_mul_f32_e32 v144, 0xbe0293ee, v174
	v_fmamk_f32 v80, v80, 0x3e0293ee, v144
	v_fmamk_f32 v81, v81, 0x3e0293ee, v144
	v_fmamk_f32 v82, v82, 0x3e0293ee, v144
	v_fmamk_f32 v83, v83, 0x3e0293ee, v144
	v_fmamk_f32 v84, v84, 0x3e0293ee, v144
	v_fmamk_f32 v85, v85, 0x3e0293ee, v144
	v_fmamk_f32 v86, v86, 0x3e0293ee, v144
	v_fmamk_f32 v87, v87, 0x3e0293ee, v144
	v_fmamk_f32 v88, v88, 0x3e0293ee, v144
	v_fmamk_f32 v89, v89, 0x3e0293ee, v144
	v_fmamk_f32 v90, v90, 0x3e0293ee, v144
	v_fmamk_f32 v91, v91, 0x3e0293ee, v144
	v_fmamk_f32 v92, v92, 0x3e0293ee, v144
	v_fmamk_f32 v93, v93, 0x3e0293ee, v144
	v_fmamk_f32 v94, v94, 0x3e0293ee, v144
	v_fmamk_f32 v95, v95, 0x3e0293ee, v144
	v_exp_f32_e32 v141, v80
	v_exp_f32_e32 v143, v81
	v_exp_f32_e32 v139, v82
	v_exp_f32_e32 v142, v83
	v_exp_f32_e32 v137, v84
	v_exp_f32_e32 v140, v85
	v_exp_f32_e32 v136, v86
	v_exp_f32_e32 v138, v87
	v_exp_f32_e32 v133, v88
	v_exp_f32_e32 v135, v89
	v_exp_f32_e32 v131, v90
	v_exp_f32_e32 v134, v91
	v_exp_f32_e32 v129, v92
	v_exp_f32_e32 v132, v93
	v_exp_f32_e32 v128, v94
	v_exp_f32_e32 v130, v95
	v_fmamk_f32 v145, v64, 0x3e0293ee, v144
	v_fmamk_f32 v146, v65, 0x3e0293ee, v144
	v_fmamk_f32 v147, v66, 0x3e0293ee, v144
	v_fmamk_f32 v181, v67, 0x3e0293ee, v144
	v_fmamk_f32 v182, v68, 0x3e0293ee, v144
	v_fmamk_f32 v183, v69, 0x3e0293ee, v144
	v_fmamk_f32 v184, v70, 0x3e0293ee, v144
	v_fmamk_f32 v185, v71, 0x3e0293ee, v144
	v_fmamk_f32 v186, v72, 0x3e0293ee, v144
	v_fmamk_f32 v187, v73, 0x3e0293ee, v144
	v_fmamk_f32 v188, v74, 0x3e0293ee, v144
	v_fmamk_f32 v189, v75, 0x3e0293ee, v144
	v_fmamk_f32 v190, v76, 0x3e0293ee, v144
	v_fmamk_f32 v191, v77, 0x3e0293ee, v144
	v_fmamk_f32 v200, v78, 0x3e0293ee, v144
	v_fmac_f32_e32 v144, 0x3e0293ee, v79
	s_waitcnt lgkmcnt(0)
	s_barrier
	s_add_i32 s2, s5, s25
	s_addk_i32 s2, 0xff40
	s_add_i32 s3, s2, 0x5e
	s_sub_i32 s2, s2, 0x5e
	v_cmp_lt_i32_e32 vcc, s3, v175
	v_cmp_gt_i32_e64 s[2:3], s2, v176
	s_nop 1
	s_or_b64 s[2:3], vcc, s[2:3]
	s_and_b64 s[2:3], s[2:3], s[8:9]
	s_cmp_eq_u64 s[2:3], exec
	s_cbranch_scc1 .Lwin_deadB
	ds_read_b128 v[64:67], v166 offset:32768
	ds_read_b128 v[230:233], v168 offset:32768
	ds_read_b128 v[234:237], v166 offset:40960
	ds_read_b128 v[238:241], v168 offset:40960
	s_andn2_b64 vcc, exec, s[8:9]
	v_exp_f32_e32 v215, v144
	v_add_f32_e32 v144, 0, v141
	v_add_f32_e32 v144, v143, v144
	v_add_f32_e32 v144, v139, v144
	v_add_f32_e32 v144, v142, v144
	v_add_f32_e32 v144, v137, v144
	v_add_f32_e32 v144, v140, v144
	v_add_f32_e32 v144, v136, v144
	v_add_f32_e32 v144, v138, v144
	v_add_f32_e32 v144, v133, v144
	v_add_f32_e32 v144, v135, v144
	v_add_f32_e32 v144, v131, v144
	v_add_f32_e32 v144, v134, v144
	v_exp_f32_e32 v201, v145
	v_add_f32_e32 v144, v129, v144
	v_exp_f32_e32 v205, v146
	v_add_f32_e32 v144, v132, v144
	v_exp_f32_e32 v206, v147
	v_add_f32_e32 v144, v128, v144
	v_exp_f32_e32 v181, v181
	v_add_f32_e32 v144, v130, v144
	v_exp_f32_e32 v207, v182
	v_add_f32_e32 v144, v201, v144
	v_exp_f32_e32 v208, v183
	v_add_f32_e32 v144, v205, v144
	v_exp_f32_e32 v209, v184
	v_add_f32_e32 v144, v206, v144
	v_exp_f32_e32 v210, v185
	v_add_f32_e32 v144, v181, v144
	v_exp_f32_e32 v211, v186
	v_add_f32_e32 v144, v207, v144
	v_exp_f32_e32 v212, v187
	v_add_f32_e32 v144, v208, v144
	v_exp_f32_e32 v213, v188
	v_add_f32_e32 v144, v209, v144
	v_exp_f32_e32 v214, v189
	v_add_f32_e32 v144, v210, v144
	v_exp_f32_e32 v190, v190
	v_add_f32_e32 v144, v211, v144
	v_exp_f32_e32 v191, v191
	v_add_f32_e32 v144, v212, v144
	v_exp_f32_e32 v200, v200
	v_add_f32_e32 v144, v213, v144
	v_add_f32_e32 v144, v214, v144
	v_add_f32_e32 v144, v190, v144
	v_add_f32_e32 v144, v191, v144
	v_add_f32_e32 v144, v200, v144
	v_add_f32_e32 v203, v215, v144
	v_mov_b32_e32 v204, v203
	v_cvt_pk_bf16_f32 v144, v141, v143
	v_cvt_pk_bf16_f32 v145, v139, v142
	v_cvt_pk_bf16_f32 v146, v137, v140
	v_cvt_pk_bf16_f32 v147, v136, v138
	s_nop 1
	v_permlane32_swap_b32_e32 v203, v204
	v_permlane32_swap_b32_e32 v144, v146
	v_permlane32_swap_b32_e32 v145, v147
	v_cvt_pk_bf16_f32 v182, v133, v135
	v_cvt_pk_bf16_f32 v183, v131, v134
	v_cvt_pk_bf16_f32 v184, v129, v132
	v_cvt_pk_bf16_f32 v185, v128, v130
	v_cvt_pk_bf16_f32 v186, v201, v205
	v_cvt_pk_bf16_f32 v187, v206, v181
	v_cvt_pk_bf16_f32 v188, v207, v208
	v_cvt_pk_bf16_f32 v189, v209, v210
	v_cvt_pk_bf16_f32 v206, v211, v212
	v_cvt_pk_bf16_f32 v207, v213, v214
	v_cvt_pk_bf16_f32 v208, v190, v191
	v_cvt_pk_bf16_f32 v209, v200, v215
	s_nop 0
	v_permlane32_swap_b32_e32 v182, v184
	v_permlane32_swap_b32_e32 v183, v185
	v_permlane32_swap_b32_e32 v186, v188
	v_permlane32_swap_b32_e32 v187, v189
	v_permlane32_swap_b32_e32 v206, v208
	v_permlane32_swap_b32_e32 v207, v209
	s_add_i32 s2, s27, 4
	s_cmp_lt_i32 s2, s20
	s_cselect_b32 s2, 0, s20
	s_cselect_b32 s3, s19, 0x4000
	s_lshl_b32 s2, s2, 6
	s_sub_i32 s2, s3, s2
	s_add_i32 s2, s25, s2
	s_mul_i32 s8, s2, 0x2400
	s_add_u32 s2, s21, s8
	s_addc_u32 s3, s22, 0
	s_add_u32 s8, s23, s8
	s_addc_u32 s9, s24, 0
	v_lshl_add_u64 v[128:129], s[8:9], 0, v[192:193]
	v_lshl_add_u64 v[132:133], s[8:9], 0, v[152:153]
	v_lshl_add_u64 v[136:137], s[2:3], 0, v[192:193]
	v_lshl_add_u64 v[140:141], s[2:3], 0, v[152:153]
	global_load_dwordx4 v[128:131], v[128:129], off
	s_nop 0
	global_load_dwordx4 v[132:135], v[132:133], off
	s_nop 0
	global_load_dwordx4 v[136:139], v[136:137], off
	s_nop 0
	global_load_dwordx4 v[140:143], v[140:141], off
	s_waitcnt lgkmcnt(3)
	v_mfma_f32_32x32x16_bf16 v[80:95], v[64:67], v[124:127], 0
	s_waitcnt lgkmcnt(2)
	v_mfma_f32_32x32x16_bf16 v[80:95], v[230:233], v[120:123], v[80:95]
	ds_read_b128 v[230:233], v167 offset:32768
	s_waitcnt lgkmcnt(2)
	v_mfma_f32_32x32x16_bf16 v[64:79], v[234:237], v[124:127], 0
	ds_read_b128 v[234:237], v167 offset:40960
	s_waitcnt lgkmcnt(2)
	v_mfma_f32_32x32x16_bf16 v[64:79], v[238:241], v[120:123], v[64:79]
	ds_read_b128 v[238:241], v165 offset:32768
	s_waitcnt lgkmcnt(2)
	v_mfma_f32_32x32x16_bf16 v[80:95], v[230:233], v[116:119], v[80:95]
	ds_read_b128 v[230:233], v165 offset:40960
	s_waitcnt lgkmcnt(2)
	v_mfma_f32_32x32x16_bf16 v[64:79], v[234:237], v[116:119], v[64:79]
	ds_read_b128 v[234:237], v164 offset:32768
	s_waitcnt lgkmcnt(2)
	v_mfma_f32_32x32x16_bf16 v[80:95], v[238:241], v[112:115], v[80:95]
	ds_read_b128 v[238:241], v164 offset:40960
	s_waitcnt lgkmcnt(2)
	v_mfma_f32_32x32x16_bf16 v[64:79], v[230:233], v[112:115], v[64:79]
	ds_read_b128 v[230:233], v163 offset:32768
	s_waitcnt lgkmcnt(2)
	v_mfma_f32_32x32x16_bf16 v[80:95], v[234:237], v[108:111], v[80:95]
	ds_read_b128 v[234:237], v163 offset:40960
	s_waitcnt lgkmcnt(2)
	v_mfma_f32_32x32x16_bf16 v[64:79], v[238:241], v[108:111], v[64:79]
	ds_read_b128 v[238:241], v162 offset:32768
	s_waitcnt lgkmcnt(2)
	v_mfma_f32_32x32x16_bf16 v[80:95], v[230:233], v[104:107], v[80:95]
	ds_read_b128 v[230:233], v162 offset:40960
	s_waitcnt lgkmcnt(2)
	v_mfma_f32_32x32x16_bf16 v[64:79], v[234:237], v[104:107], v[64:79]
	ds_read_b128 v[234:237], v161 offset:32768
	s_waitcnt lgkmcnt(2)
	v_mfma_f32_32x32x16_bf16 v[80:95], v[238:241], v[100:103], v[80:95]
	ds_read_b128 v[238:241], v161 offset:40960
	s_waitcnt lgkmcnt(2)
	v_mfma_f32_32x32x16_bf16 v[64:79], v[230:233], v[100:103], v[64:79]
	s_waitcnt lgkmcnt(1)
	v_mfma_f32_32x32x16_bf16 v[80:95], v[234:237], v[96:99], v[80:95]
	s_waitcnt lgkmcnt(0)
	v_mfma_f32_32x32x16_bf16 v[64:79], v[238:241], v[96:99], v[64:79]
	s_cbranch_vccnz .LBB0_652
	s_add_i32 s2, s5, s25
	s_addk_i32 s2, 0xff40
	v_cmp_lt_i32_e32 vcc, s2, v175
	v_cmp_gt_i32_e64 s[2:3], s2, v176
	s_or_b64 s[8:9], vcc, s[2:3]
	s_and_saveexec_b64 s[2:3], s[8:9]
	s_cbranch_execz .LBB0_651
	v_add_u32_e32 v242, s25, v178
	v_subrev_u32_e32 v243, 64, v242
	s_movk_i32 s8, 0x101
	v_cmp_gt_u32_e32 vcc, s8, v243
	v_subrev_u32_e32 v243, 32, v242
	s_nop 0
	v_cndmask_b32_e32 v80, v217, v80, vcc
	v_cmp_gt_u32_e32 vcc, s8, v243
	v_subrev_u32_e32 v243, 63, v242
	s_nop 0
	v_cndmask_b32_e32 v64, v217, v64, vcc
	v_cmp_gt_u32_e32 vcc, s8, v243
	v_subrev_u32_e32 v243, 31, v242
	s_nop 0
	v_cndmask_b32_e32 v81, v217, v81, vcc
	v_cmp_gt_u32_e32 vcc, s8, v243
	v_subrev_u32_e32 v243, 62, v242
	s_nop 0
	v_cndmask_b32_e32 v65, v217, v65, vcc
	v_cmp_gt_u32_e32 vcc, s8, v243
	v_subrev_u32_e32 v243, 30, v242
	s_nop 0
	v_cndmask_b32_e32 v82, v217, v82, vcc
	v_cmp_gt_u32_e32 vcc, s8, v243
	v_subrev_u32_e32 v243, 61, v242
	s_nop 0
	v_cndmask_b32_e32 v66, v217, v66, vcc
	v_cmp_gt_u32_e32 vcc, s8, v243
	v_subrev_u32_e32 v243, 29, v242
	s_nop 0
	v_cndmask_b32_e32 v83, v217, v83, vcc
	v_cmp_gt_u32_e32 vcc, s8, v243
	v_subrev_u32_e32 v243, 56, v242
	s_nop 0
	v_cndmask_b32_e32 v67, v217, v67, vcc
	v_cmp_gt_u32_e32 vcc, s8, v243
	v_subrev_u32_e32 v243, 24, v242
	s_nop 0
	v_cndmask_b32_e32 v84, v217, v84, vcc
	v_cmp_gt_u32_e32 vcc, s8, v243
	v_subrev_u32_e32 v243, 55, v242
	s_nop 0
	v_cndmask_b32_e32 v68, v217, v68, vcc
	v_cmp_gt_u32_e32 vcc, s8, v243
	v_subrev_u32_e32 v243, 23, v242
	s_nop 0
	v_cndmask_b32_e32 v85, v217, v85, vcc
	v_cmp_gt_u32_e32 vcc, s8, v243
	v_subrev_u32_e32 v243, 54, v242
	s_nop 0
	v_cndmask_b32_e32 v69, v217, v69, vcc
	v_cmp_gt_u32_e32 vcc, s8, v243
	v_subrev_u32_e32 v243, 22, v242
	s_nop 0
	v_cndmask_b32_e32 v86, v217, v86, vcc
	v_cmp_gt_u32_e32 vcc, s8, v243
	v_subrev_u32_e32 v243, 53, v242
	s_nop 0
	v_cndmask_b32_e32 v70, v217, v70, vcc
	v_cmp_gt_u32_e32 vcc, s8, v243
	v_subrev_u32_e32 v243, 21, v242
	s_nop 0
	v_cndmask_b32_e32 v87, v217, v87, vcc
	v_cmp_gt_u32_e32 vcc, s8, v243
	v_subrev_u32_e32 v243, 48, v242
	s_nop 0
	v_cndmask_b32_e32 v71, v217, v71, vcc
	v_cmp_gt_u32_e32 vcc, s8, v243
	v_add_u32_e32 v243, -16, v242
	s_nop 0
	v_cndmask_b32_e32 v88, v217, v88, vcc
	v_cmp_gt_u32_e32 vcc, s8, v243
	v_subrev_u32_e32 v243, 47, v242
	s_nop 0
	v_cndmask_b32_e32 v72, v217, v72, vcc
	v_cmp_gt_u32_e32 vcc, s8, v243
	v_add_u32_e32 v243, -15, v242
	s_nop 0
	v_cndmask_b32_e32 v89, v217, v89, vcc
	v_cmp_gt_u32_e32 vcc, s8, v243
	v_subrev_u32_e32 v243, 46, v242
	s_nop 0
	v_cndmask_b32_e32 v73, v217, v73, vcc
	v_cmp_gt_u32_e32 vcc, s8, v243
	v_add_u32_e32 v243, -14, v242
	s_nop 0
	v_cndmask_b32_e32 v90, v217, v90, vcc
	v_cmp_gt_u32_e32 vcc, s8, v243
	v_subrev_u32_e32 v243, 45, v242
	s_nop 0
	v_cndmask_b32_e32 v74, v217, v74, vcc
	v_cmp_gt_u32_e32 vcc, s8, v243
	v_add_u32_e32 v243, -13, v242
	s_nop 0
	v_cndmask_b32_e32 v91, v217, v91, vcc
	v_cmp_gt_u32_e32 vcc, s8, v243
	v_subrev_u32_e32 v243, 40, v242
	s_nop 0
	v_cndmask_b32_e32 v75, v217, v75, vcc
	v_cmp_gt_u32_e32 vcc, s8, v243
	v_add_u32_e32 v243, -8, v242
	s_nop 0
	v_cndmask_b32_e32 v92, v217, v92, vcc
	v_cmp_gt_u32_e32 vcc, s8, v243
	v_subrev_u32_e32 v243, 39, v242
	s_nop 0
	v_cndmask_b32_e32 v76, v217, v76, vcc
	v_cmp_gt_u32_e32 vcc, s8, v243
	v_add_u32_e32 v243, -7, v242
	s_nop 0
	v_cndmask_b32_e32 v93, v217, v93, vcc
	v_cmp_gt_u32_e32 vcc, s8, v243
	v_subrev_u32_e32 v243, 38, v242
	s_nop 0
	v_cndmask_b32_e32 v77, v217, v77, vcc
	v_cmp_gt_u32_e32 vcc, s8, v243
	v_add_u32_e32 v243, -6, v242
	s_nop 0
	v_cndmask_b32_e32 v94, v217, v94, vcc
	v_cmp_gt_u32_e32 vcc, s8, v243
	v_subrev_u32_e32 v243, 37, v242
	v_add_u32_e32 v242, -5, v242
	v_cndmask_b32_e32 v78, v217, v78, vcc
	v_cmp_gt_u32_e32 vcc, s8, v243
	s_nop 1
	v_cndmask_b32_e32 v95, v217, v95, vcc
	v_cmp_gt_u32_e32 vcc, s8, v242
	s_nop 1
	v_cndmask_b32_e32 v79, v217, v79, vcc

.Lwin_deadA:
	v_add_f32_e32 v144, 0, v191
	v_add_f32_e32 v144, v201, v144
	v_add_f32_e32 v144, v145, v144
	v_add_f32_e32 v144, v200, v144
	v_add_f32_e32 v144, v146, v144
	v_add_f32_e32 v144, v190, v144
	v_add_f32_e32 v144, v147, v144
	v_add_f32_e32 v144, v189, v144
	v_add_f32_e32 v144, v186, v144
	v_add_f32_e32 v144, v188, v144
	v_add_f32_e32 v144, v185, v144
	v_add_f32_e32 v144, v187, v144
	v_exp_f32_e32 v142, v142
	v_add_f32_e32 v144, v182, v144
	v_exp_f32_e32 v143, v143
	v_add_f32_e32 v144, v184, v144
	v_exp_f32_e32 v140, v140
	v_add_f32_e32 v144, v181, v144
	v_exp_f32_e32 v141, v141
	v_add_f32_e32 v144, v183, v144
	v_exp_f32_e32 v138, v138
	v_add_f32_e32 v144, v142, v144
	v_exp_f32_e32 v139, v139
	v_add_f32_e32 v144, v143, v144
	v_exp_f32_e32 v136, v136
	v_add_f32_e32 v144, v140, v144
	v_exp_f32_e32 v137, v137
	v_add_f32_e32 v144, v141, v144
	v_exp_f32_e32 v134, v134
	v_add_f32_e32 v144, v138, v144
	v_exp_f32_e32 v135, v135
	v_add_f32_e32 v144, v139, v144
	v_exp_f32_e32 v132, v132
	v_add_f32_e32 v144, v136, v144
	v_exp_f32_e32 v133, v133
	v_add_f32_e32 v144, v137, v144
	v_exp_f32_e32 v130, v130
	v_add_f32_e32 v144, v134, v144
	v_exp_f32_e32 v131, v131
	v_add_f32_e32 v144, v135, v144
	v_exp_f32_e32 v128, v128
	v_add_f32_e32 v144, v132, v144
	v_exp_f32_e32 v129, v129
	v_add_f32_e32 v144, v133, v144
	v_add_f32_e32 v144, v130, v144
	v_add_f32_e32 v144, v131, v144
	v_add_f32_e32 v144, v128, v144
	v_add_f32_e32 v179, v129, v144
	v_mov_b32_e32 v180, v179
	v_cvt_pk_bf16_f32 v144, v191, v201
	v_cvt_pk_bf16_f32 v145, v145, v200
	v_cvt_pk_bf16_f32 v146, v146, v190
	v_cvt_pk_bf16_f32 v147, v147, v189
	v_cvt_pk_bf16_f32 v186, v186, v188
	v_cvt_pk_bf16_f32 v187, v185, v187
	v_cvt_pk_bf16_f32 v188, v182, v184
	v_cvt_pk_bf16_f32 v189, v181, v183
	v_cvt_pk_bf16_f32 v182, v142, v143
	v_cvt_pk_bf16_f32 v183, v140, v141
	v_cvt_pk_bf16_f32 v184, v138, v139
	v_cvt_pk_bf16_f32 v185, v136, v137
	v_cvt_pk_bf16_f32 v200, v134, v135
	v_cvt_pk_bf16_f32 v201, v132, v133
	v_cvt_pk_bf16_f32 v202, v130, v131
	s_nop 0
	v_permlane32_swap_b32_e32 v179, v180
	v_permlane32_swap_b32_e32 v144, v146
	v_cvt_pk_bf16_f32 v203, v128, v129
	v_permlane32_swap_b32_e32 v200, v202
	v_permlane32_swap_b32_e32 v145, v147
	v_permlane32_swap_b32_e32 v186, v188
	v_permlane32_swap_b32_e32 v187, v189
	v_permlane32_swap_b32_e32 v182, v184
	v_permlane32_swap_b32_e32 v183, v185
	v_permlane32_swap_b32_e32 v201, v203
	s_add_i32 s2, s27, 3
	s_cmp_lt_i32 s2, s20
	s_cselect_b64 s[8:9], -1, 0
	s_and_b64 s[2:3], s[8:9], exec
	s_cselect_b32 s2, 0, s20
	s_cselect_b32 s3, s19, 0x4000
	s_lshl_b32 s2, s2, 6
	s_sub_i32 s2, s3, s2
	s_add_i32 s2, s25, s2
	s_mulk_i32 s2, 0x2400
	s_add_i32 s10, s2, 0xfff70000
	s_add_u32 s2, s21, s10
	s_addc_u32 s3, s22, 0
	s_add_u32 s10, s23, s10
	s_addc_u32 s11, s24, 0
	v_lshl_add_u64 v[128:129], s[10:11], 0, v[192:193]
	v_lshl_add_u64 v[132:133], s[10:11], 0, v[152:153]
	v_lshl_add_u64 v[136:137], s[2:3], 0, v[192:193]
	v_lshl_add_u64 v[140:141], s[2:3], 0, v[152:153]
	global_load_dwordx4 v[128:131], v[128:129], off
	s_nop 0
	global_load_dwordx4 v[132:135], v[132:133], off
	s_nop 0
	global_load_dwordx4 v[136:139], v[136:137], off
	s_nop 0
	global_load_dwordx4 v[140:143], v[140:141], off
	v_mov_b32_e32 v64, v217
	v_mov_b32_e32 v65, v217
	v_mov_b32_e32 v66, v217
	v_mov_b32_e32 v67, v217
	v_mov_b32_e32 v68, v217
	v_mov_b32_e32 v69, v217
	v_mov_b32_e32 v70, v217
	v_mov_b32_e32 v71, v217
	v_mov_b32_e32 v72, v217
	v_mov_b32_e32 v73, v217
	v_mov_b32_e32 v74, v217
	v_mov_b32_e32 v75, v217
	v_mov_b32_e32 v76, v217
	v_mov_b32_e32 v77, v217
	v_mov_b32_e32 v78, v217
	v_mov_b32_e32 v79, v217
	v_mov_b32_e32 v80, v217
	v_mov_b32_e32 v81, v217
	v_mov_b32_e32 v82, v217
	v_mov_b32_e32 v83, v217
	v_mov_b32_e32 v84, v217
	v_mov_b32_e32 v85, v217
	v_mov_b32_e32 v86, v217
	v_mov_b32_e32 v87, v217
	v_mov_b32_e32 v88, v217
	v_mov_b32_e32 v89, v217
	v_mov_b32_e32 v90, v217
	v_mov_b32_e32 v91, v217
	v_mov_b32_e32 v92, v217
	v_mov_b32_e32 v93, v217
	v_mov_b32_e32 v94, v217
	v_mov_b32_e32 v95, v217
	s_branch .LBB0_644
.Lwin_deadB:
	s_andn2_b64 vcc, exec, s[8:9]
	v_exp_f32_e32 v215, v144
	v_add_f32_e32 v144, 0, v141
	v_add_f32_e32 v144, v143, v144
	v_add_f32_e32 v144, v139, v144
	v_add_f32_e32 v144, v142, v144
	v_add_f32_e32 v144, v137, v144
	v_add_f32_e32 v144, v140, v144
	v_add_f32_e32 v144, v136, v144
	v_add_f32_e32 v144, v138, v144
	v_add_f32_e32 v144, v133, v144
	v_add_f32_e32 v144, v135, v144
	v_add_f32_e32 v144, v131, v144
	v_add_f32_e32 v144, v134, v144
	v_exp_f32_e32 v201, v145
	v_add_f32_e32 v144, v129, v144
	v_exp_f32_e32 v205, v146
	v_add_f32_e32 v144, v132, v144
	v_exp_f32_e32 v206, v147
	v_add_f32_e32 v144, v128, v144
	v_exp_f32_e32 v181, v181
	v_add_f32_e32 v144, v130, v144
	v_exp_f32_e32 v207, v182
	v_add_f32_e32 v144, v201, v144
	v_exp_f32_e32 v208, v183
	v_add_f32_e32 v144, v205, v144
	v_exp_f32_e32 v209, v184
	v_add_f32_e32 v144, v206, v144
	v_exp_f32_e32 v210, v185
	v_add_f32_e32 v144, v181, v144
	v_exp_f32_e32 v211, v186
	v_add_f32_e32 v144, v207, v144
	v_exp_f32_e32 v212, v187
	v_add_f32_e32 v144, v208, v144
	v_exp_f32_e32 v213, v188
	v_add_f32_e32 v144, v209, v144
	v_exp_f32_e32 v214, v189
	v_add_f32_e32 v144, v210, v144
	v_exp_f32_e32 v190, v190
	v_add_f32_e32 v144, v211, v144
	v_exp_f32_e32 v191, v191
	v_add_f32_e32 v144, v212, v144
	v_exp_f32_e32 v200, v200
	v_add_f32_e32 v144, v213, v144
	v_add_f32_e32 v144, v214, v144
	v_add_f32_e32 v144, v190, v144
	v_add_f32_e32 v144, v191, v144
	v_add_f32_e32 v144, v200, v144
	v_add_f32_e32 v203, v215, v144
	v_mov_b32_e32 v204, v203
	v_cvt_pk_bf16_f32 v144, v141, v143
	v_cvt_pk_bf16_f32 v145, v139, v142
	v_cvt_pk_bf16_f32 v146, v137, v140
	v_cvt_pk_bf16_f32 v147, v136, v138
	s_nop 1
	v_permlane32_swap_b32_e32 v203, v204
	v_permlane32_swap_b32_e32 v144, v146
	v_permlane32_swap_b32_e32 v145, v147
	v_cvt_pk_bf16_f32 v182, v133, v135
	v_cvt_pk_bf16_f32 v183, v131, v134
	v_cvt_pk_bf16_f32 v184, v129, v132
	v_cvt_pk_bf16_f32 v185, v128, v130
	v_cvt_pk_bf16_f32 v186, v201, v205
	v_cvt_pk_bf16_f32 v187, v206, v181
	v_cvt_pk_bf16_f32 v188, v207, v208
	v_cvt_pk_bf16_f32 v189, v209, v210
	v_cvt_pk_bf16_f32 v206, v211, v212
	v_cvt_pk_bf16_f32 v207, v213, v214
	v_cvt_pk_bf16_f32 v208, v190, v191
	v_cvt_pk_bf16_f32 v209, v200, v215
	s_nop 0
	v_permlane32_swap_b32_e32 v182, v184
	v_permlane32_swap_b32_e32 v183, v185
	v_permlane32_swap_b32_e32 v186, v188
	v_permlane32_swap_b32_e32 v187, v189
	v_permlane32_swap_b32_e32 v206, v208
	v_permlane32_swap_b32_e32 v207, v209
	s_add_i32 s2, s27, 4
	s_cmp_lt_i32 s2, s20
	s_cselect_b32 s2, 0, s20
	s_cselect_b32 s3, s19, 0x4000
	s_lshl_b32 s2, s2, 6
	s_sub_i32 s2, s3, s2
	s_add_i32 s2, s25, s2
	s_mul_i32 s8, s2, 0x2400
	s_add_u32 s2, s21, s8
	s_addc_u32 s3, s22, 0
	s_add_u32 s8, s23, s8
	s_addc_u32 s9, s24, 0
	v_lshl_add_u64 v[128:129], s[8:9], 0, v[192:193]
	v_lshl_add_u64 v[132:133], s[8:9], 0, v[152:153]
	v_lshl_add_u64 v[136:137], s[2:3], 0, v[192:193]
	v_lshl_add_u64 v[140:141], s[2:3], 0, v[152:153]
	global_load_dwordx4 v[128:131], v[128:129], off
	s_nop 0
	global_load_dwordx4 v[132:135], v[132:133], off
	s_nop 0
	global_load_dwordx4 v[136:139], v[136:137], off
	s_nop 0
	global_load_dwordx4 v[140:143], v[140:141], off
	v_mov_b32_e32 v64, v217
	v_mov_b32_e32 v65, v217
	v_mov_b32_e32 v66, v217
	v_mov_b32_e32 v67, v217
	v_mov_b32_e32 v68, v217
	v_mov_b32_e32 v69, v217
	v_mov_b32_e32 v70, v217
	v_mov_b32_e32 v71, v217
	v_mov_b32_e32 v72, v217
	v_mov_b32_e32 v73, v217
	v_mov_b32_e32 v74, v217
	v_mov_b32_e32 v75, v217
	v_mov_b32_e32 v76, v217
	v_mov_b32_e32 v77, v217
	v_mov_b32_e32 v78, v217
	v_mov_b32_e32 v79, v217
	v_mov_b32_e32 v80, v217
	v_mov_b32_e32 v81, v217
	v_mov_b32_e32 v82, v217
	v_mov_b32_e32 v83, v217
	v_mov_b32_e32 v84, v217
	v_mov_b32_e32 v85, v217
	v_mov_b32_e32 v86, v217
	v_mov_b32_e32 v87, v217
	v_mov_b32_e32 v88, v217
	v_mov_b32_e32 v89, v217
	v_mov_b32_e32 v90, v217
	v_mov_b32_e32 v91, v217
	v_mov_b32_e32 v92, v217
	v_mov_b32_e32 v93, v217
	v_mov_b32_e32 v94, v217
	v_mov_b32_e32 v95, v217
	s_branch .LBB0_652
